# prologue weight conversion: 4-iteration load loops fully unrolled (32 loads in flight per wave instead of 8)
# baseline (speedup 1.0000x reference)
.LBB0_41:
	v_lshl_add_u64 v[68:69], v[44:45], 0, s[6:7]
	v_lshl_add_u64 v[70:71], v[42:43], 0, s[6:7]
	v_lshl_add_u64 v[72:73], v[40:41], 0, s[6:7]
	v_lshl_add_u64 v[74:75], v[38:39], 0, s[6:7]
	v_lshl_add_u64 v[76:77], v[36:37], 0, s[6:7]
	v_lshl_add_u64 v[78:79], v[34:35], 0, s[6:7]
	v_lshl_add_u64 v[80:81], v[32:33], 0, s[6:7]
	v_lshl_add_u64 v[82:83], v[30:31], 0, s[6:7]
	global_load_dword v120, v[68:69], off nt
	global_load_dword v121, v[70:71], off nt
	global_load_dword v122, v[72:73], off nt
	global_load_dword v123, v[74:75], off nt
	global_load_dword v124, v[76:77], off nt
	global_load_dword v125, v[78:79], off nt
	global_load_dword v126, v[80:81], off nt
	global_load_dword v127, v[82:83], off nt
	s_add_u32 s6, s6, 0x10000
	s_addc_u32 s7, s7, 0
	v_lshl_add_u64 v[152:153], v[44:45], 0, s[6:7]
	v_lshl_add_u64 v[154:155], v[42:43], 0, s[6:7]
	v_lshl_add_u64 v[156:157], v[40:41], 0, s[6:7]
	v_lshl_add_u64 v[158:159], v[38:39], 0, s[6:7]
	v_lshl_add_u64 v[160:161], v[36:37], 0, s[6:7]
	v_lshl_add_u64 v[162:163], v[34:35], 0, s[6:7]
	v_lshl_add_u64 v[164:165], v[32:33], 0, s[6:7]
	v_lshl_add_u64 v[166:167], v[30:31], 0, s[6:7]
	global_load_dword v128, v[152:153], off nt
	global_load_dword v129, v[154:155], off nt
	global_load_dword v130, v[156:157], off nt
	global_load_dword v131, v[158:159], off nt
	global_load_dword v132, v[160:161], off nt
	global_load_dword v133, v[162:163], off nt
	global_load_dword v134, v[164:165], off nt
	global_load_dword v135, v[166:167], off nt
	s_add_u32 s6, s6, 0x10000
	s_addc_u32 s7, s7, 0
	v_lshl_add_u64 v[168:169], v[44:45], 0, s[6:7]
	v_lshl_add_u64 v[170:171], v[42:43], 0, s[6:7]
	v_lshl_add_u64 v[172:173], v[40:41], 0, s[6:7]
	v_lshl_add_u64 v[174:175], v[38:39], 0, s[6:7]
	v_lshl_add_u64 v[176:177], v[36:37], 0, s[6:7]
	v_lshl_add_u64 v[178:179], v[34:35], 0, s[6:7]
	v_lshl_add_u64 v[180:181], v[32:33], 0, s[6:7]
	v_lshl_add_u64 v[182:183], v[30:31], 0, s[6:7]
	global_load_dword v136, v[168:169], off nt
	global_load_dword v137, v[170:171], off nt
	global_load_dword v138, v[172:173], off nt
	global_load_dword v139, v[174:175], off nt
	global_load_dword v140, v[176:177], off nt
	global_load_dword v141, v[178:179], off nt
	global_load_dword v142, v[180:181], off nt
	global_load_dword v143, v[182:183], off nt
	s_add_u32 s6, s6, 0x10000
	s_addc_u32 s7, s7, 0
	v_lshl_add_u64 v[184:185], v[44:45], 0, s[6:7]
	v_lshl_add_u64 v[186:187], v[42:43], 0, s[6:7]
	v_lshl_add_u64 v[188:189], v[40:41], 0, s[6:7]
	v_lshl_add_u64 v[190:191], v[38:39], 0, s[6:7]
	v_lshl_add_u64 v[192:193], v[36:37], 0, s[6:7]
	v_lshl_add_u64 v[194:195], v[34:35], 0, s[6:7]
	v_lshl_add_u64 v[196:197], v[32:33], 0, s[6:7]
	v_lshl_add_u64 v[198:199], v[30:31], 0, s[6:7]
	global_load_dword v144, v[184:185], off nt
	global_load_dword v145, v[186:187], off nt
	global_load_dword v146, v[188:189], off nt
	global_load_dword v147, v[190:191], off nt
	global_load_dword v148, v[192:193], off nt
	global_load_dword v149, v[194:195], off nt
	global_load_dword v150, v[196:197], off nt
	global_load_dword v151, v[198:199], off nt
	s_add_u32 s6, s6, 0x10000
	s_addc_u32 s7, s7, 0
	v_add_u32_e32 v75, 0x400, v8
	s_waitcnt vmcnt(31)
	v_mul_f32_e32 v120, 0x42800000, v120
	s_waitcnt vmcnt(30)
	v_mul_f32_e32 v121, 0x42800000, v121
	s_waitcnt vmcnt(29)
	v_mul_f32_e32 v122, 0x42800000, v122
	s_waitcnt vmcnt(28)
	v_mul_f32_e32 v123, 0x42800000, v123
	s_waitcnt vmcnt(27)
	v_mul_f32_e32 v124, 0x42800000, v124
	s_waitcnt vmcnt(26)
	v_mul_f32_e32 v125, 0x42800000, v125
	s_waitcnt vmcnt(25)
	v_mul_f32_e32 v126, 0x42800000, v126
	s_waitcnt vmcnt(24)
	v_mul_f32_e32 v127, 0x42800000, v127
	ds_write2_b32 v8, v120, v121 offset1:66
	ds_write2_b32 v8, v122, v123 offset0:132 offset1:198
	ds_write2_b32 v75, v124, v125 offset0:8 offset1:74
	ds_write2_b32 v75, v126, v127 offset0:140 offset1:206
	v_add_u32_e32 v8, 0x840, v8
	v_add_u32_e32 v75, 0x400, v8
	s_waitcnt vmcnt(23)
	v_mul_f32_e32 v128, 0x42800000, v128
	s_waitcnt vmcnt(22)
	v_mul_f32_e32 v129, 0x42800000, v129
	s_waitcnt vmcnt(21)
	v_mul_f32_e32 v130, 0x42800000, v130
	s_waitcnt vmcnt(20)
	v_mul_f32_e32 v131, 0x42800000, v131
	s_waitcnt vmcnt(19)
	v_mul_f32_e32 v132, 0x42800000, v132
	s_waitcnt vmcnt(18)
	v_mul_f32_e32 v133, 0x42800000, v133
	s_waitcnt vmcnt(17)
	v_mul_f32_e32 v134, 0x42800000, v134
	s_waitcnt vmcnt(16)
	v_mul_f32_e32 v135, 0x42800000, v135
	ds_write2_b32 v8, v128, v129 offset1:66
	ds_write2_b32 v8, v130, v131 offset0:132 offset1:198
	ds_write2_b32 v75, v132, v133 offset0:8 offset1:74
	ds_write2_b32 v75, v134, v135 offset0:140 offset1:206
	v_add_u32_e32 v8, 0x840, v8
	v_add_u32_e32 v75, 0x400, v8
	s_waitcnt vmcnt(15)
	v_mul_f32_e32 v136, 0x42800000, v136
	s_waitcnt vmcnt(14)
	v_mul_f32_e32 v137, 0x42800000, v137
	s_waitcnt vmcnt(13)
	v_mul_f32_e32 v138, 0x42800000, v138
	s_waitcnt vmcnt(12)
	v_mul_f32_e32 v139, 0x42800000, v139
	s_waitcnt vmcnt(11)
	v_mul_f32_e32 v140, 0x42800000, v140
	s_waitcnt vmcnt(10)
	v_mul_f32_e32 v141, 0x42800000, v141
	s_waitcnt vmcnt(9)
	v_mul_f32_e32 v142, 0x42800000, v142
	s_waitcnt vmcnt(8)
	v_mul_f32_e32 v143, 0x42800000, v143
	ds_write2_b32 v8, v136, v137 offset1:66
	ds_write2_b32 v8, v138, v139 offset0:132 offset1:198
	ds_write2_b32 v75, v140, v141 offset0:8 offset1:74
	ds_write2_b32 v75, v142, v143 offset0:140 offset1:206
	v_add_u32_e32 v8, 0x840, v8
	v_add_u32_e32 v75, 0x400, v8
	s_waitcnt vmcnt(7)
	v_mul_f32_e32 v144, 0x42800000, v144
	s_waitcnt vmcnt(6)
	v_mul_f32_e32 v145, 0x42800000, v145
	s_waitcnt vmcnt(5)
	v_mul_f32_e32 v146, 0x42800000, v146
	s_waitcnt vmcnt(4)
	v_mul_f32_e32 v147, 0x42800000, v147
	s_waitcnt vmcnt(3)
	v_mul_f32_e32 v148, 0x42800000, v148
	s_waitcnt vmcnt(2)
	v_mul_f32_e32 v149, 0x42800000, v149
	s_waitcnt vmcnt(1)
	v_mul_f32_e32 v150, 0x42800000, v150
	s_waitcnt vmcnt(0)
	v_mul_f32_e32 v151, 0x42800000, v151
	ds_write2_b32 v8, v144, v145 offset1:66
	ds_write2_b32 v8, v146, v147 offset0:132 offset1:198
	ds_write2_b32 v75, v148, v149 offset0:8 offset1:74
	ds_write2_b32 v75, v150, v151 offset0:140 offset1:206
	v_add_u32_e32 v8, 0x840, v8
	s_cmp_lg_u32 s6, 0x40000
	s_waitcnt lgkmcnt(0)
	ds_read2_b32 v[34:35], v3 offset1:16
	ds_read2_b32 v[36:37], v3 offset0:33 offset1:49
	ds_read2_b32 v[40:41], v3 offset0:66 offset1:82
	ds_read2_b32 v[42:43], v3 offset0:99 offset1:115
	v_mov_b32_e32 v30, v9
	ds_read2_b32 v[44:45], v3 offset0:132 offset1:148
	ds_read2_b32 v[68:69], v3 offset0:165 offset1:181
	s_waitcnt lgkmcnt(5)
	v_med3_f32 v8, v34, s38, v66
	s_waitcnt lgkmcnt(4)
	v_med3_f32 v31, v36, s38, v66
	v_cvt_pk_fp8_f32 v30, v8, v31
	s_waitcnt lgkmcnt(3)
	v_med3_f32 v8, v40, s38, v66
	s_waitcnt lgkmcnt(2)
	v_med3_f32 v31, v42, s38, v66
	ds_read2_b32 v[70:71], v3 offset0:198 offset1:214
	ds_read2_b32 v[72:73], v3 offset0:231 offset1:247
	v_add_u32_e32 v33, 0x400, v3
	v_cvt_pk_fp8_f32 v30, v8, v31 op_sel:[0,0,1]
	s_waitcnt lgkmcnt(3)
	v_med3_f32 v8, v44, s38, v66
	s_waitcnt lgkmcnt(2)
	v_med3_f32 v32, v68, s38, v66
	v_mov_b32_e32 v31, v9
	ds_read2_b32 v[74:75], v33 offset0:8 offset1:24
	ds_read2_b32 v[76:77], v33 offset0:41 offset1:57
	v_cvt_pk_fp8_f32 v31, v8, v32
	ds_read2_b32 v[78:79], v33 offset0:74 offset1:90
	ds_read2_b32 v[80:81], v33 offset0:107 offset1:123
	ds_read2_b32 v[82:83], v33 offset0:140 offset1:156
	ds_read2_b32 v[84:85], v33 offset0:173 offset1:189
	s_waitcnt lgkmcnt(7)
	v_med3_f32 v8, v70, s38, v66
	s_waitcnt lgkmcnt(6)
	v_med3_f32 v32, v72, s38, v66
	v_cvt_pk_fp8_f32 v31, v8, v32 op_sel:[0,0,1]
	s_waitcnt lgkmcnt(5)
	v_med3_f32 v8, v74, s38, v66
	s_waitcnt lgkmcnt(4)
	v_med3_f32 v34, v76, s38, v66
	v_mov_b32_e32 v32, v9
	ds_read2_b32 v[86:87], v33 offset0:206 offset1:222
	ds_read2_b32 v[88:89], v33 offset0:239 offset1:255
	v_cvt_pk_fp8_f32 v32, v8, v34
	s_waitcnt lgkmcnt(3)
	v_med3_f32 v36, v82, s38, v66
	s_waitcnt lgkmcnt(2)
	v_med3_f32 v40, v84, s38, v66
	v_mov_b32_e32 v33, v9
	s_lshl_b32 s0, s11, 5
	v_cvt_pk_fp8_f32 v33, v36, v40
	s_and_b32 s0, s0, 0x3e0
	s_mul_i32 s9, s9, 0x380000
	s_add_u32 s6, s20, s9
	v_med3_f32 v8, v78, s38, v66
	v_med3_f32 v34, v80, s38, v66
	s_addc_u32 s7, s21, 0
	v_cvt_pk_fp8_f32 v32, v8, v34 op_sel:[0,0,1]
	s_waitcnt lgkmcnt(1)
	v_med3_f32 v8, v86, s38, v66
	s_waitcnt lgkmcnt(0)
	v_med3_f32 v34, v88, s38, v66
	s_add_u32 s6, s6, s10
	v_cvt_pk_fp8_f32 v33, v8, v34 op_sel:[0,0,1]
	s_addc_u32 s7, s7, 0
	v_lshl_add_u64 v[38:39], s[6:7], 0, v[6:7]
	v_add_u32_e32 v8, s0, v1
	v_mad_i64_i32 v[90:91], s[6:7], v8, s39, v[38:39]
	global_store_dwordx4 v[90:91], v[30:33], off nt
	v_med3_f32 v8, v35, s38, v66
	v_med3_f32 v34, v69, s38, v66
	v_med3_f32 v31, v37, s38, v66
	v_mov_b32_e32 v30, v9
	v_cvt_pk_fp8_f32 v30, v8, v31
	v_med3_f32 v33, v45, s38, v66
	v_mov_b32_e32 v31, v9
	v_cvt_pk_fp8_f32 v31, v33, v34
	v_med3_f32 v8, v41, s38, v66
	v_med3_f32 v32, v43, s38, v66
	v_cvt_pk_fp8_f32 v30, v8, v32 op_sel:[0,0,1]
	v_med3_f32 v8, v71, s38, v66
	v_med3_f32 v32, v73, s38, v66
	v_cvt_pk_fp8_f32 v31, v8, v32 op_sel:[0,0,1]
	v_med3_f32 v8, v75, s38, v66
	v_med3_f32 v33, v77, s38, v66
	v_mov_b32_e32 v32, v9
	v_cvt_pk_fp8_f32 v32, v8, v33
	v_med3_f32 v35, v83, s38, v66
	v_med3_f32 v36, v85, s38, v66
	v_mov_b32_e32 v33, v9
	v_cvt_pk_fp8_f32 v33, v35, v36
	v_med3_f32 v8, v79, s38, v66
	v_med3_f32 v34, v81, s38, v66
	v_cvt_pk_fp8_f32 v32, v8, v34 op_sel:[0,0,1]
	v_med3_f32 v8, v87, s38, v66
	v_med3_f32 v34, v89, s38, v66
	v_cvt_pk_fp8_f32 v33, v8, v34 op_sel:[0,0,1]
	v_add_u32_e32 v8, s0, v13
	v_mad_i64_i32 v[34:35], s[6:7], v8, s39, v[38:39]
	global_store_dwordx4 v[34:35], v[30:33], off nt
	s_waitcnt lgkmcnt(0)
	s_mov_b64 s[6:7], 0

.LBB0_45:
	v_lshl_add_u64 v[68:69], v[44:45], 0, s[6:7]
	v_lshl_add_u64 v[70:71], v[42:43], 0, s[6:7]
	v_lshl_add_u64 v[72:73], v[40:41], 0, s[6:7]
	v_lshl_add_u64 v[74:75], v[38:39], 0, s[6:7]
	v_lshl_add_u64 v[76:77], v[36:37], 0, s[6:7]
	v_lshl_add_u64 v[78:79], v[34:35], 0, s[6:7]
	v_lshl_add_u64 v[80:81], v[32:33], 0, s[6:7]
	v_lshl_add_u64 v[82:83], v[30:31], 0, s[6:7]
	global_load_dword v120, v[68:69], off nt
	global_load_dword v121, v[70:71], off nt
	global_load_dword v122, v[72:73], off nt
	global_load_dword v123, v[74:75], off nt
	global_load_dword v124, v[76:77], off nt
	global_load_dword v125, v[78:79], off nt
	global_load_dword v126, v[80:81], off nt
	global_load_dword v127, v[82:83], off nt
	s_add_u32 s6, s6, 0x38000
	s_addc_u32 s7, s7, 0
	v_lshl_add_u64 v[152:153], v[44:45], 0, s[6:7]
	v_lshl_add_u64 v[154:155], v[42:43], 0, s[6:7]
	v_lshl_add_u64 v[156:157], v[40:41], 0, s[6:7]
	v_lshl_add_u64 v[158:159], v[38:39], 0, s[6:7]
	v_lshl_add_u64 v[160:161], v[36:37], 0, s[6:7]
	v_lshl_add_u64 v[162:163], v[34:35], 0, s[6:7]
	v_lshl_add_u64 v[164:165], v[32:33], 0, s[6:7]
	v_lshl_add_u64 v[166:167], v[30:31], 0, s[6:7]
	global_load_dword v128, v[152:153], off nt
	global_load_dword v129, v[154:155], off nt
	global_load_dword v130, v[156:157], off nt
	global_load_dword v131, v[158:159], off nt
	global_load_dword v132, v[160:161], off nt
	global_load_dword v133, v[162:163], off nt
	global_load_dword v134, v[164:165], off nt
	global_load_dword v135, v[166:167], off nt
	s_add_u32 s6, s6, 0x38000
	s_addc_u32 s7, s7, 0
	v_lshl_add_u64 v[168:169], v[44:45], 0, s[6:7]
	v_lshl_add_u64 v[170:171], v[42:43], 0, s[6:7]
	v_lshl_add_u64 v[172:173], v[40:41], 0, s[6:7]
	v_lshl_add_u64 v[174:175], v[38:39], 0, s[6:7]
	v_lshl_add_u64 v[176:177], v[36:37], 0, s[6:7]
	v_lshl_add_u64 v[178:179], v[34:35], 0, s[6:7]
	v_lshl_add_u64 v[180:181], v[32:33], 0, s[6:7]
	v_lshl_add_u64 v[182:183], v[30:31], 0, s[6:7]
	global_load_dword v136, v[168:169], off nt
	global_load_dword v137, v[170:171], off nt
	global_load_dword v138, v[172:173], off nt
	global_load_dword v139, v[174:175], off nt
	global_load_dword v140, v[176:177], off nt
	global_load_dword v141, v[178:179], off nt
	global_load_dword v142, v[180:181], off nt
	global_load_dword v143, v[182:183], off nt
	s_add_u32 s6, s6, 0x38000
	s_addc_u32 s7, s7, 0
	v_lshl_add_u64 v[184:185], v[44:45], 0, s[6:7]
	v_lshl_add_u64 v[186:187], v[42:43], 0, s[6:7]
	v_lshl_add_u64 v[188:189], v[40:41], 0, s[6:7]
	v_lshl_add_u64 v[190:191], v[38:39], 0, s[6:7]
	v_lshl_add_u64 v[192:193], v[36:37], 0, s[6:7]
	v_lshl_add_u64 v[194:195], v[34:35], 0, s[6:7]
	v_lshl_add_u64 v[196:197], v[32:33], 0, s[6:7]
	v_lshl_add_u64 v[198:199], v[30:31], 0, s[6:7]
	global_load_dword v144, v[184:185], off nt
	global_load_dword v145, v[186:187], off nt
	global_load_dword v146, v[188:189], off nt
	global_load_dword v147, v[190:191], off nt
	global_load_dword v148, v[192:193], off nt
	global_load_dword v149, v[194:195], off nt
	global_load_dword v150, v[196:197], off nt
	global_load_dword v151, v[198:199], off nt
	s_add_u32 s6, s6, 0x38000
	s_addc_u32 s7, s7, 0
	v_add_u32_e32 v75, 0x400, v8
	s_waitcnt vmcnt(31)
	v_mul_f32_e32 v120, 0x42800000, v120
	s_waitcnt vmcnt(30)
	v_mul_f32_e32 v121, 0x42800000, v121
	s_waitcnt vmcnt(29)
	v_mul_f32_e32 v122, 0x42800000, v122
	s_waitcnt vmcnt(28)
	v_mul_f32_e32 v123, 0x42800000, v123
	s_waitcnt vmcnt(27)
	v_mul_f32_e32 v124, 0x42800000, v124
	s_waitcnt vmcnt(26)
	v_mul_f32_e32 v125, 0x42800000, v125
	s_waitcnt vmcnt(25)
	v_mul_f32_e32 v126, 0x42800000, v126
	s_waitcnt vmcnt(24)
	v_mul_f32_e32 v127, 0x42800000, v127
	ds_write2_b32 v8, v120, v121 offset1:66
	ds_write2_b32 v8, v122, v123 offset0:132 offset1:198
	ds_write2_b32 v75, v124, v125 offset0:8 offset1:74
	ds_write2_b32 v75, v126, v127 offset0:140 offset1:206
	v_add_u32_e32 v8, 0x840, v8
	v_add_u32_e32 v75, 0x400, v8
	s_waitcnt vmcnt(23)
	v_mul_f32_e32 v128, 0x42800000, v128
	s_waitcnt vmcnt(22)
	v_mul_f32_e32 v129, 0x42800000, v129
	s_waitcnt vmcnt(21)
	v_mul_f32_e32 v130, 0x42800000, v130
	s_waitcnt vmcnt(20)
	v_mul_f32_e32 v131, 0x42800000, v131
	s_waitcnt vmcnt(19)
	v_mul_f32_e32 v132, 0x42800000, v132
	s_waitcnt vmcnt(18)
	v_mul_f32_e32 v133, 0x42800000, v133
	s_waitcnt vmcnt(17)
	v_mul_f32_e32 v134, 0x42800000, v134
	s_waitcnt vmcnt(16)
	v_mul_f32_e32 v135, 0x42800000, v135
	ds_write2_b32 v8, v128, v129 offset1:66
	ds_write2_b32 v8, v130, v131 offset0:132 offset1:198
	ds_write2_b32 v75, v132, v133 offset0:8 offset1:74
	ds_write2_b32 v75, v134, v135 offset0:140 offset1:206
	v_add_u32_e32 v8, 0x840, v8
	v_add_u32_e32 v75, 0x400, v8
	s_waitcnt vmcnt(15)
	v_mul_f32_e32 v136, 0x42800000, v136
	s_waitcnt vmcnt(14)
	v_mul_f32_e32 v137, 0x42800000, v137
	s_waitcnt vmcnt(13)
	v_mul_f32_e32 v138, 0x42800000, v138
	s_waitcnt vmcnt(12)
	v_mul_f32_e32 v139, 0x42800000, v139
	s_waitcnt vmcnt(11)
	v_mul_f32_e32 v140, 0x42800000, v140
	s_waitcnt vmcnt(10)
	v_mul_f32_e32 v141, 0x42800000, v141
	s_waitcnt vmcnt(9)
	v_mul_f32_e32 v142, 0x42800000, v142
	s_waitcnt vmcnt(8)
	v_mul_f32_e32 v143, 0x42800000, v143
	ds_write2_b32 v8, v136, v137 offset1:66
	ds_write2_b32 v8, v138, v139 offset0:132 offset1:198
	ds_write2_b32 v75, v140, v141 offset0:8 offset1:74
	ds_write2_b32 v75, v142, v143 offset0:140 offset1:206
	v_add_u32_e32 v8, 0x840, v8
	v_add_u32_e32 v75, 0x400, v8
	s_waitcnt vmcnt(7)
	v_mul_f32_e32 v144, 0x42800000, v144
	s_waitcnt vmcnt(6)
	v_mul_f32_e32 v145, 0x42800000, v145
	s_waitcnt vmcnt(5)
	v_mul_f32_e32 v146, 0x42800000, v146
	s_waitcnt vmcnt(4)
	v_mul_f32_e32 v147, 0x42800000, v147
	s_waitcnt vmcnt(3)
	v_mul_f32_e32 v148, 0x42800000, v148
	s_waitcnt vmcnt(2)
	v_mul_f32_e32 v149, 0x42800000, v149
	s_waitcnt vmcnt(1)
	v_mul_f32_e32 v150, 0x42800000, v150
	s_waitcnt vmcnt(0)
	v_mul_f32_e32 v151, 0x42800000, v151
	ds_write2_b32 v8, v144, v145 offset1:66
	ds_write2_b32 v8, v146, v147 offset0:132 offset1:198
	ds_write2_b32 v75, v148, v149 offset0:8 offset1:74
	ds_write2_b32 v75, v150, v151 offset0:140 offset1:206
	v_add_u32_e32 v8, 0x840, v8
	s_cmp_lg_u32 s6, 0xe0000
	s_waitcnt lgkmcnt(0)
	ds_read2_b32 v[34:35], v3 offset1:16
	ds_read2_b32 v[36:37], v3 offset0:33 offset1:49
	ds_read2_b32 v[40:41], v3 offset0:66 offset1:82
	ds_read2_b32 v[42:43], v3 offset0:99 offset1:115
	v_mov_b32_e32 v30, v9
	ds_read2_b32 v[44:45], v3 offset0:132 offset1:148
	ds_read2_b32 v[68:69], v3 offset0:165 offset1:181
	s_waitcnt lgkmcnt(5)
	v_med3_f32 v8, v34, s38, v66
	s_waitcnt lgkmcnt(4)
	v_med3_f32 v31, v36, s38, v66
	v_cvt_pk_fp8_f32 v30, v8, v31
	s_waitcnt lgkmcnt(3)
	v_med3_f32 v8, v40, s38, v66
	s_waitcnt lgkmcnt(2)
	v_med3_f32 v31, v42, s38, v66
	ds_read2_b32 v[70:71], v3 offset0:198 offset1:214
	ds_read2_b32 v[72:73], v3 offset0:231 offset1:247
	v_add_u32_e32 v33, 0x400, v3
	v_cvt_pk_fp8_f32 v30, v8, v31 op_sel:[0,0,1]
	s_waitcnt lgkmcnt(3)
	v_med3_f32 v8, v44, s38, v66
	s_waitcnt lgkmcnt(2)
	v_med3_f32 v32, v68, s38, v66
	v_mov_b32_e32 v31, v9
	ds_read2_b32 v[74:75], v33 offset0:8 offset1:24
	ds_read2_b32 v[76:77], v33 offset0:41 offset1:57
	v_cvt_pk_fp8_f32 v31, v8, v32
	ds_read2_b32 v[78:79], v33 offset0:74 offset1:90
	ds_read2_b32 v[80:81], v33 offset0:107 offset1:123
	ds_read2_b32 v[82:83], v33 offset0:140 offset1:156
	ds_read2_b32 v[84:85], v33 offset0:173 offset1:189
	s_waitcnt lgkmcnt(7)
	v_med3_f32 v8, v70, s38, v66
	s_waitcnt lgkmcnt(6)
	v_med3_f32 v32, v72, s38, v66
	v_cvt_pk_fp8_f32 v31, v8, v32 op_sel:[0,0,1]
	s_waitcnt lgkmcnt(5)
	v_med3_f32 v8, v74, s38, v66
	s_waitcnt lgkmcnt(4)
	v_med3_f32 v34, v76, s38, v66
	v_mov_b32_e32 v32, v9
	ds_read2_b32 v[86:87], v33 offset0:206 offset1:222
	ds_read2_b32 v[88:89], v33 offset0:239 offset1:255
	v_cvt_pk_fp8_f32 v32, v8, v34
	s_waitcnt lgkmcnt(3)
	v_med3_f32 v36, v82, s38, v66
	s_waitcnt lgkmcnt(2)
	v_med3_f32 v40, v84, s38, v66
	v_mov_b32_e32 v33, v9
	v_cvt_pk_fp8_f32 v33, v36, v40
	s_mul_i32 s9, s9, 0x700000
	s_and_b32 s0, s10, 0x1fe0
	s_add_u32 s6, s22, s9
	v_med3_f32 v8, v78, s38, v66
	v_med3_f32 v34, v80, s38, v66
	s_addc_u32 s7, s23, 0
	v_cvt_pk_fp8_f32 v32, v8, v34 op_sel:[0,0,1]
	s_waitcnt lgkmcnt(1)
	v_med3_f32 v8, v86, s38, v66
	s_waitcnt lgkmcnt(0)
	v_med3_f32 v34, v88, s38, v66
	s_add_u32 s6, s6, s11
	v_cvt_pk_fp8_f32 v33, v8, v34 op_sel:[0,0,1]
	v_add_u32_e32 v90, s0, v1
	s_addc_u32 s7, s7, 0
	v_ashrrev_i32_e32 v91, 31, v90
	v_lshl_add_u64 v[38:39], s[6:7], 0, v[6:7]
	v_lshlrev_b64 v[90:91], 10, v[90:91]
	v_lshl_add_u64 v[90:91], v[38:39], 0, v[90:91]
	global_store_dwordx4 v[90:91], v[30:33], off nt
	v_med3_f32 v8, v35, s38, v66
	v_med3_f32 v34, v69, s38, v66
	v_med3_f32 v31, v37, s38, v66
	v_mov_b32_e32 v30, v9
	v_cvt_pk_fp8_f32 v30, v8, v31
	v_med3_f32 v33, v45, s38, v66
	v_mov_b32_e32 v31, v9
	v_cvt_pk_fp8_f32 v31, v33, v34
	v_med3_f32 v8, v41, s38, v66
	v_med3_f32 v32, v43, s38, v66
	v_cvt_pk_fp8_f32 v30, v8, v32 op_sel:[0,0,1]
	v_med3_f32 v8, v71, s38, v66
	v_med3_f32 v32, v73, s38, v66
	v_cvt_pk_fp8_f32 v31, v8, v32 op_sel:[0,0,1]
	v_med3_f32 v8, v75, s38, v66
	v_med3_f32 v33, v77, s38, v66
	v_mov_b32_e32 v32, v9
	v_cvt_pk_fp8_f32 v32, v8, v33
	v_med3_f32 v35, v83, s38, v66
	v_med3_f32 v36, v85, s38, v66
	v_mov_b32_e32 v33, v9
	v_cvt_pk_fp8_f32 v33, v35, v36
	v_med3_f32 v8, v79, s38, v66
	v_med3_f32 v34, v81, s38, v66
	v_cvt_pk_fp8_f32 v32, v8, v34 op_sel:[0,0,1]
	v_med3_f32 v8, v87, s38, v66
	v_med3_f32 v34, v89, s38, v66
	v_cvt_pk_fp8_f32 v33, v8, v34 op_sel:[0,0,1]
	v_add_u32_e32 v34, s0, v13
	v_ashrrev_i32_e32 v35, 31, v34
	v_lshlrev_b64 v[34:35], 10, v[34:35]
	v_lshl_add_u64 v[34:35], v[38:39], 0, v[34:35]
	global_store_dwordx4 v[34:35], v[30:33], off nt
	s_waitcnt lgkmcnt(0)

.LBB0_50:
	v_lshl_add_u64 v[68:69], v[44:45], 0, s[6:7]
	v_lshl_add_u64 v[70:71], v[42:43], 0, s[6:7]
	v_lshl_add_u64 v[72:73], v[40:41], 0, s[6:7]
	v_lshl_add_u64 v[74:75], v[38:39], 0, s[6:7]
	v_lshl_add_u64 v[76:77], v[36:37], 0, s[6:7]
	v_lshl_add_u64 v[78:79], v[34:35], 0, s[6:7]
	v_lshl_add_u64 v[80:81], v[32:33], 0, s[6:7]
	v_lshl_add_u64 v[82:83], v[30:31], 0, s[6:7]
	global_load_dword v120, v[68:69], off nt
	global_load_dword v121, v[70:71], off nt
	global_load_dword v122, v[72:73], off nt
	global_load_dword v123, v[74:75], off nt
	global_load_dword v124, v[76:77], off nt
	global_load_dword v125, v[78:79], off nt
	global_load_dword v126, v[80:81], off nt
	global_load_dword v127, v[82:83], off nt
	s_add_u32 s6, s6, 0x10000
	s_addc_u32 s7, s7, 0
	v_lshl_add_u64 v[152:153], v[44:45], 0, s[6:7]
	v_lshl_add_u64 v[154:155], v[42:43], 0, s[6:7]
	v_lshl_add_u64 v[156:157], v[40:41], 0, s[6:7]
	v_lshl_add_u64 v[158:159], v[38:39], 0, s[6:7]
	v_lshl_add_u64 v[160:161], v[36:37], 0, s[6:7]
	v_lshl_add_u64 v[162:163], v[34:35], 0, s[6:7]
	v_lshl_add_u64 v[164:165], v[32:33], 0, s[6:7]
	v_lshl_add_u64 v[166:167], v[30:31], 0, s[6:7]
	global_load_dword v128, v[152:153], off nt
	global_load_dword v129, v[154:155], off nt
	global_load_dword v130, v[156:157], off nt
	global_load_dword v131, v[158:159], off nt
	global_load_dword v132, v[160:161], off nt
	global_load_dword v133, v[162:163], off nt
	global_load_dword v134, v[164:165], off nt
	global_load_dword v135, v[166:167], off nt
	s_add_u32 s6, s6, 0x10000
	s_addc_u32 s7, s7, 0
	v_lshl_add_u64 v[168:169], v[44:45], 0, s[6:7]
	v_lshl_add_u64 v[170:171], v[42:43], 0, s[6:7]
	v_lshl_add_u64 v[172:173], v[40:41], 0, s[6:7]
	v_lshl_add_u64 v[174:175], v[38:39], 0, s[6:7]
	v_lshl_add_u64 v[176:177], v[36:37], 0, s[6:7]
	v_lshl_add_u64 v[178:179], v[34:35], 0, s[6:7]
	v_lshl_add_u64 v[180:181], v[32:33], 0, s[6:7]
	v_lshl_add_u64 v[182:183], v[30:31], 0, s[6:7]
	global_load_dword v136, v[168:169], off nt
	global_load_dword v137, v[170:171], off nt
	global_load_dword v138, v[172:173], off nt
	global_load_dword v139, v[174:175], off nt
	global_load_dword v140, v[176:177], off nt
	global_load_dword v141, v[178:179], off nt
	global_load_dword v142, v[180:181], off nt
	global_load_dword v143, v[182:183], off nt
	s_add_u32 s6, s6, 0x10000
	s_addc_u32 s7, s7, 0
	v_lshl_add_u64 v[184:185], v[44:45], 0, s[6:7]
	v_lshl_add_u64 v[186:187], v[42:43], 0, s[6:7]
	v_lshl_add_u64 v[188:189], v[40:41], 0, s[6:7]
	v_lshl_add_u64 v[190:191], v[38:39], 0, s[6:7]
	v_lshl_add_u64 v[192:193], v[36:37], 0, s[6:7]
	v_lshl_add_u64 v[194:195], v[34:35], 0, s[6:7]
	v_lshl_add_u64 v[196:197], v[32:33], 0, s[6:7]
	v_lshl_add_u64 v[198:199], v[30:31], 0, s[6:7]
	global_load_dword v144, v[184:185], off nt
	global_load_dword v145, v[186:187], off nt
	global_load_dword v146, v[188:189], off nt
	global_load_dword v147, v[190:191], off nt
	global_load_dword v148, v[192:193], off nt
	global_load_dword v149, v[194:195], off nt
	global_load_dword v150, v[196:197], off nt
	global_load_dword v151, v[198:199], off nt
	s_add_u32 s6, s6, 0x10000
	s_addc_u32 s7, s7, 0
	v_add_u32_e32 v75, 0x400, v8
	s_waitcnt vmcnt(31)
	v_mul_f32_e32 v120, 0x42800000, v120
	s_waitcnt vmcnt(30)
	v_mul_f32_e32 v121, 0x42800000, v121
	s_waitcnt vmcnt(29)
	v_mul_f32_e32 v122, 0x42800000, v122
	s_waitcnt vmcnt(28)
	v_mul_f32_e32 v123, 0x42800000, v123
	s_waitcnt vmcnt(27)
	v_mul_f32_e32 v124, 0x42800000, v124
	s_waitcnt vmcnt(26)
	v_mul_f32_e32 v125, 0x42800000, v125
	s_waitcnt vmcnt(25)
	v_mul_f32_e32 v126, 0x42800000, v126
	s_waitcnt vmcnt(24)
	v_mul_f32_e32 v127, 0x42800000, v127
	ds_write2_b32 v8, v120, v121 offset1:66
	ds_write2_b32 v8, v122, v123 offset0:132 offset1:198
	ds_write2_b32 v75, v124, v125 offset0:8 offset1:74
	ds_write2_b32 v75, v126, v127 offset0:140 offset1:206
	v_add_u32_e32 v8, 0x840, v8
	v_add_u32_e32 v75, 0x400, v8
	s_waitcnt vmcnt(23)
	v_mul_f32_e32 v128, 0x42800000, v128
	s_waitcnt vmcnt(22)
	v_mul_f32_e32 v129, 0x42800000, v129
	s_waitcnt vmcnt(21)
	v_mul_f32_e32 v130, 0x42800000, v130
	s_waitcnt vmcnt(20)
	v_mul_f32_e32 v131, 0x42800000, v131
	s_waitcnt vmcnt(19)
	v_mul_f32_e32 v132, 0x42800000, v132
	s_waitcnt vmcnt(18)
	v_mul_f32_e32 v133, 0x42800000, v133
	s_waitcnt vmcnt(17)
	v_mul_f32_e32 v134, 0x42800000, v134
	s_waitcnt vmcnt(16)
	v_mul_f32_e32 v135, 0x42800000, v135
	ds_write2_b32 v8, v128, v129 offset1:66
	ds_write2_b32 v8, v130, v131 offset0:132 offset1:198
	ds_write2_b32 v75, v132, v133 offset0:8 offset1:74
	ds_write2_b32 v75, v134, v135 offset0:140 offset1:206
	v_add_u32_e32 v8, 0x840, v8
	v_add_u32_e32 v75, 0x400, v8
	s_waitcnt vmcnt(15)
	v_mul_f32_e32 v136, 0x42800000, v136
	s_waitcnt vmcnt(14)
	v_mul_f32_e32 v137, 0x42800000, v137
	s_waitcnt vmcnt(13)
	v_mul_f32_e32 v138, 0x42800000, v138
	s_waitcnt vmcnt(12)
	v_mul_f32_e32 v139, 0x42800000, v139
	s_waitcnt vmcnt(11)
	v_mul_f32_e32 v140, 0x42800000, v140
	s_waitcnt vmcnt(10)
	v_mul_f32_e32 v141, 0x42800000, v141
	s_waitcnt vmcnt(9)
	v_mul_f32_e32 v142, 0x42800000, v142
	s_waitcnt vmcnt(8)
	v_mul_f32_e32 v143, 0x42800000, v143
	ds_write2_b32 v8, v136, v137 offset1:66
	ds_write2_b32 v8, v138, v139 offset0:132 offset1:198
	ds_write2_b32 v75, v140, v141 offset0:8 offset1:74
	ds_write2_b32 v75, v142, v143 offset0:140 offset1:206
	v_add_u32_e32 v8, 0x840, v8
	v_add_u32_e32 v75, 0x400, v8
	s_waitcnt vmcnt(7)
	v_mul_f32_e32 v144, 0x42800000, v144
	s_waitcnt vmcnt(6)
	v_mul_f32_e32 v145, 0x42800000, v145
	s_waitcnt vmcnt(5)
	v_mul_f32_e32 v146, 0x42800000, v146
	s_waitcnt vmcnt(4)
	v_mul_f32_e32 v147, 0x42800000, v147
	s_waitcnt vmcnt(3)
	v_mul_f32_e32 v148, 0x42800000, v148
	s_waitcnt vmcnt(2)
	v_mul_f32_e32 v149, 0x42800000, v149
	s_waitcnt vmcnt(1)
	v_mul_f32_e32 v150, 0x42800000, v150
	s_waitcnt vmcnt(0)
	v_mul_f32_e32 v151, 0x42800000, v151
	ds_write2_b32 v8, v144, v145 offset1:66
	ds_write2_b32 v8, v146, v147 offset0:132 offset1:198
	ds_write2_b32 v75, v148, v149 offset0:8 offset1:74
	ds_write2_b32 v75, v150, v151 offset0:140 offset1:206
	v_add_u32_e32 v8, 0x840, v8
	s_cmp_lg_u32 s6, 0x40000
	s_waitcnt lgkmcnt(0)
	ds_read2_b32 v[34:35], v3 offset1:16
	ds_read2_b32 v[36:37], v3 offset0:33 offset1:49
	ds_read2_b32 v[40:41], v3 offset0:66 offset1:82
	ds_read2_b32 v[42:43], v3 offset0:99 offset1:115
	v_mov_b32_e32 v30, v9
	ds_read2_b32 v[44:45], v3 offset0:132 offset1:148
	ds_read2_b32 v[68:69], v3 offset0:165 offset1:181
	s_waitcnt lgkmcnt(5)
	v_med3_f32 v8, v34, s38, v66
	s_waitcnt lgkmcnt(4)
	v_med3_f32 v31, v36, s38, v66
	v_cvt_pk_fp8_f32 v30, v8, v31
	s_waitcnt lgkmcnt(3)
	v_med3_f32 v8, v40, s38, v66
	s_waitcnt lgkmcnt(2)
	v_med3_f32 v31, v42, s38, v66
	ds_read2_b32 v[70:71], v3 offset0:198 offset1:214
	ds_read2_b32 v[72:73], v3 offset0:231 offset1:247
	v_add_u32_e32 v33, 0x400, v3
	v_cvt_pk_fp8_f32 v30, v8, v31 op_sel:[0,0,1]
	s_waitcnt lgkmcnt(3)
	v_med3_f32 v8, v44, s38, v66
	s_waitcnt lgkmcnt(2)
	v_med3_f32 v32, v68, s38, v66
	v_mov_b32_e32 v31, v9
	ds_read2_b32 v[74:75], v33 offset0:8 offset1:24
	ds_read2_b32 v[76:77], v33 offset0:41 offset1:57
	v_cvt_pk_fp8_f32 v31, v8, v32
	ds_read2_b32 v[78:79], v33 offset0:74 offset1:90
	ds_read2_b32 v[80:81], v33 offset0:107 offset1:123
	ds_read2_b32 v[82:83], v33 offset0:140 offset1:156
	ds_read2_b32 v[84:85], v33 offset0:173 offset1:189
	s_waitcnt lgkmcnt(7)
	v_med3_f32 v8, v70, s38, v66
	s_waitcnt lgkmcnt(6)
	v_med3_f32 v32, v72, s38, v66
	v_cvt_pk_fp8_f32 v31, v8, v32 op_sel:[0,0,1]
	s_waitcnt lgkmcnt(5)
	v_med3_f32 v8, v74, s38, v66
	s_waitcnt lgkmcnt(4)
	v_med3_f32 v34, v76, s38, v66
	v_mov_b32_e32 v32, v9
	ds_read2_b32 v[86:87], v33 offset0:206 offset1:222
	ds_read2_b32 v[88:89], v33 offset0:239 offset1:255
	v_cvt_pk_fp8_f32 v32, v8, v34
	s_waitcnt lgkmcnt(3)
	v_med3_f32 v36, v82, s38, v66
	s_waitcnt lgkmcnt(2)
	v_med3_f32 v40, v84, s38, v66
	v_mov_b32_e32 v33, v9
	v_cvt_pk_fp8_f32 v33, v36, v40
	v_med3_f32 v8, v78, s38, v66
	v_med3_f32 v34, v80, s38, v66
	s_lshl_b32 s0, s46, 1
	v_cvt_pk_fp8_f32 v32, v8, v34 op_sel:[0,0,1]
	s_waitcnt lgkmcnt(1)
	v_med3_f32 v8, v86, s38, v66
	s_waitcnt lgkmcnt(0)
	v_med3_f32 v34, v88, s38, v66
	s_and_b32 s0, s0, 0x3fc0
	s_lshl_b32 s6, s46, 5
	v_cvt_pk_fp8_f32 v33, v8, v34 op_sel:[0,0,1]
	s_addk_i32 s0, 0xd000
	s_and_b32 s9, s6, 0x3e0
	v_lshl_add_u64 v[38:39], v[10:11], 0, s[0:1]
	v_add_u32_e32 v8, s9, v1
	v_mad_i64_i32 v[90:91], s[6:7], v8, s40, v[38:39]
	global_store_dwordx4 v[90:91], v[30:33], off nt
	v_med3_f32 v8, v35, s38, v66
	v_med3_f32 v34, v69, s38, v66
	v_med3_f32 v31, v37, s38, v66
	v_mov_b32_e32 v30, v9
	v_cvt_pk_fp8_f32 v30, v8, v31
	v_med3_f32 v33, v45, s38, v66
	v_mov_b32_e32 v31, v9
	v_cvt_pk_fp8_f32 v31, v33, v34
	v_med3_f32 v8, v41, s38, v66
	v_med3_f32 v32, v43, s38, v66
	v_cvt_pk_fp8_f32 v30, v8, v32 op_sel:[0,0,1]
	v_med3_f32 v8, v71, s38, v66
	v_med3_f32 v32, v73, s38, v66
	v_cvt_pk_fp8_f32 v31, v8, v32 op_sel:[0,0,1]
	v_med3_f32 v8, v75, s38, v66
	v_med3_f32 v33, v77, s38, v66
	v_mov_b32_e32 v32, v9
	v_cvt_pk_fp8_f32 v32, v8, v33
	v_med3_f32 v35, v83, s38, v66
	v_med3_f32 v36, v85, s38, v66
	v_mov_b32_e32 v33, v9
	v_cvt_pk_fp8_f32 v33, v35, v36
	v_med3_f32 v8, v79, s38, v66
	v_med3_f32 v34, v81, s38, v66
	v_cvt_pk_fp8_f32 v32, v8, v34 op_sel:[0,0,1]
	v_med3_f32 v8, v87, s38, v66
	v_med3_f32 v34, v89, s38, v66
	v_cvt_pk_fp8_f32 v33, v8, v34 op_sel:[0,0,1]
	v_add_u32_e32 v8, s9, v13
	v_mad_i64_i32 v[34:35], s[6:7], v8, s40, v[38:39]
	global_store_dwordx4 v[34:35], v[30:33], off nt
	s_waitcnt lgkmcnt(0)

.LBB0_55:
	v_lshl_add_u64 v[68:69], v[44:45], 0, s[6:7]
	v_lshl_add_u64 v[70:71], v[42:43], 0, s[6:7]
	v_lshl_add_u64 v[72:73], v[40:41], 0, s[6:7]
	v_lshl_add_u64 v[74:75], v[38:39], 0, s[6:7]
	v_lshl_add_u64 v[76:77], v[36:37], 0, s[6:7]
	v_lshl_add_u64 v[78:79], v[34:35], 0, s[6:7]
	v_lshl_add_u64 v[80:81], v[32:33], 0, s[6:7]
	v_lshl_add_u64 v[82:83], v[30:31], 0, s[6:7]
	global_load_dword v120, v[68:69], off nt
	global_load_dword v121, v[70:71], off nt
	global_load_dword v122, v[72:73], off nt
	global_load_dword v123, v[74:75], off nt
	global_load_dword v124, v[76:77], off nt
	global_load_dword v125, v[78:79], off nt
	global_load_dword v126, v[80:81], off nt
	global_load_dword v127, v[82:83], off nt
	s_add_u32 s6, s6, 0x2c000
	s_addc_u32 s7, s7, 0
	v_lshl_add_u64 v[152:153], v[44:45], 0, s[6:7]
	v_lshl_add_u64 v[154:155], v[42:43], 0, s[6:7]
	v_lshl_add_u64 v[156:157], v[40:41], 0, s[6:7]
	v_lshl_add_u64 v[158:159], v[38:39], 0, s[6:7]
	v_lshl_add_u64 v[160:161], v[36:37], 0, s[6:7]
	v_lshl_add_u64 v[162:163], v[34:35], 0, s[6:7]
	v_lshl_add_u64 v[164:165], v[32:33], 0, s[6:7]
	v_lshl_add_u64 v[166:167], v[30:31], 0, s[6:7]
	global_load_dword v128, v[152:153], off nt
	global_load_dword v129, v[154:155], off nt
	global_load_dword v130, v[156:157], off nt
	global_load_dword v131, v[158:159], off nt
	global_load_dword v132, v[160:161], off nt
	global_load_dword v133, v[162:163], off nt
	global_load_dword v134, v[164:165], off nt
	global_load_dword v135, v[166:167], off nt
	s_add_u32 s6, s6, 0x2c000
	s_addc_u32 s7, s7, 0
	v_lshl_add_u64 v[168:169], v[44:45], 0, s[6:7]
	v_lshl_add_u64 v[170:171], v[42:43], 0, s[6:7]
	v_lshl_add_u64 v[172:173], v[40:41], 0, s[6:7]
	v_lshl_add_u64 v[174:175], v[38:39], 0, s[6:7]
	v_lshl_add_u64 v[176:177], v[36:37], 0, s[6:7]
	v_lshl_add_u64 v[178:179], v[34:35], 0, s[6:7]
	v_lshl_add_u64 v[180:181], v[32:33], 0, s[6:7]
	v_lshl_add_u64 v[182:183], v[30:31], 0, s[6:7]
	global_load_dword v136, v[168:169], off nt
	global_load_dword v137, v[170:171], off nt
	global_load_dword v138, v[172:173], off nt
	global_load_dword v139, v[174:175], off nt
	global_load_dword v140, v[176:177], off nt
	global_load_dword v141, v[178:179], off nt
	global_load_dword v142, v[180:181], off nt
	global_load_dword v143, v[182:183], off nt
	s_add_u32 s6, s6, 0x2c000
	s_addc_u32 s7, s7, 0
	v_lshl_add_u64 v[184:185], v[44:45], 0, s[6:7]
	v_lshl_add_u64 v[186:187], v[42:43], 0, s[6:7]
	v_lshl_add_u64 v[188:189], v[40:41], 0, s[6:7]
	v_lshl_add_u64 v[190:191], v[38:39], 0, s[6:7]
	v_lshl_add_u64 v[192:193], v[36:37], 0, s[6:7]
	v_lshl_add_u64 v[194:195], v[34:35], 0, s[6:7]
	v_lshl_add_u64 v[196:197], v[32:33], 0, s[6:7]
	v_lshl_add_u64 v[198:199], v[30:31], 0, s[6:7]
	global_load_dword v144, v[184:185], off nt
	global_load_dword v145, v[186:187], off nt
	global_load_dword v146, v[188:189], off nt
	global_load_dword v147, v[190:191], off nt
	global_load_dword v148, v[192:193], off nt
	global_load_dword v149, v[194:195], off nt
	global_load_dword v150, v[196:197], off nt
	global_load_dword v151, v[198:199], off nt
	s_add_u32 s6, s6, 0x2c000
	s_addc_u32 s7, s7, 0
	v_add_u32_e32 v75, 0x400, v8
	s_waitcnt vmcnt(30)
	ds_write2_b32 v8, v120, v121 offset1:66
	s_waitcnt vmcnt(28)
	ds_write2_b32 v8, v122, v123 offset0:132 offset1:198
	s_waitcnt vmcnt(26)
	ds_write2_b32 v75, v124, v125 offset0:8 offset1:74
	s_waitcnt vmcnt(24)
	ds_write2_b32 v75, v126, v127 offset0:140 offset1:206
	v_add_u32_e32 v8, 0x840, v8
	v_add_u32_e32 v75, 0x400, v8
	s_waitcnt vmcnt(22)
	ds_write2_b32 v8, v128, v129 offset1:66
	s_waitcnt vmcnt(20)
	ds_write2_b32 v8, v130, v131 offset0:132 offset1:198
	s_waitcnt vmcnt(18)
	ds_write2_b32 v75, v132, v133 offset0:8 offset1:74
	s_waitcnt vmcnt(16)
	ds_write2_b32 v75, v134, v135 offset0:140 offset1:206
	v_add_u32_e32 v8, 0x840, v8
	v_add_u32_e32 v75, 0x400, v8
	s_waitcnt vmcnt(14)
	ds_write2_b32 v8, v136, v137 offset1:66
	s_waitcnt vmcnt(12)
	ds_write2_b32 v8, v138, v139 offset0:132 offset1:198
	s_waitcnt vmcnt(10)
	ds_write2_b32 v75, v140, v141 offset0:8 offset1:74
	s_waitcnt vmcnt(8)
	ds_write2_b32 v75, v142, v143 offset0:140 offset1:206
	v_add_u32_e32 v8, 0x840, v8
	v_add_u32_e32 v75, 0x400, v8
	s_waitcnt vmcnt(6)
	ds_write2_b32 v8, v144, v145 offset1:66
	s_waitcnt vmcnt(4)
	ds_write2_b32 v8, v146, v147 offset0:132 offset1:198
	s_waitcnt vmcnt(2)
	ds_write2_b32 v75, v148, v149 offset0:8 offset1:74
	s_waitcnt vmcnt(0)
	ds_write2_b32 v75, v150, v151 offset0:140 offset1:206
	v_add_u32_e32 v8, 0x840, v8
	s_cmp_lg_u32 s6, 0xb0000
	s_waitcnt lgkmcnt(0)
	ds_read2_b32 v[34:35], v47 offset1:8
	ds_read2_b32 v[38:39], v47 offset0:33 offset1:41
	ds_read2_b32 v[40:41], v47 offset0:66 offset1:74
	ds_read2_b32 v[42:43], v47 offset0:99 offset1:107
	ds_read2_b32 v[44:45], v47 offset0:132 offset1:140
	s_waitcnt lgkmcnt(4)
	s_waitcnt lgkmcnt(3)
	ds_read2_b32 v[68:69], v47 offset0:165 offset1:173
	v_cvt_pk_bf16_f32 v30, v34, v38
	s_waitcnt lgkmcnt(3)
	s_waitcnt lgkmcnt(2)
	ds_read2_b32 v[70:71], v47 offset0:198 offset1:206
	ds_read2_b32 v[72:73], v47 offset0:231 offset1:239
	s_lshl_b32 s0, s46, 1
	v_cvt_pk_bf16_f32 v31, v40, v42
	s_waitcnt lgkmcnt(3)
	s_and_b32 s0, s0, 0x3fe0
	s_waitcnt lgkmcnt(2)
	s_add_i32 s6, s0, 0xffffe600
	s_lshl_b32 s0, s46, 7
	v_cvt_pk_bf16_f32 v32, v44, v68
	s_waitcnt lgkmcnt(1)
	v_add_u32_e32 v74, s6, v46
	s_and_b32 s0, s0, 0x780
	s_waitcnt lgkmcnt(0)
	v_ashrrev_i32_e32 v75, 31, v74
	v_lshl_add_u64 v[36:37], v[14:15], 0, s[0:1]
	v_lshlrev_b64 v[74:75], 11, v[74:75]
	v_cvt_pk_bf16_f32 v33, v70, v72
	v_lshl_add_u64 v[74:75], v[36:37], 0, v[74:75]
	global_store_dwordx4 v[74:75], v[30:33], off
	s_nop 1
	v_cvt_pk_bf16_f32 v30, v35, v39
	v_cvt_pk_bf16_f32 v31, v41, v43
	v_cvt_pk_bf16_f32 v32, v45, v69
	v_add_u32_e32 v34, s6, v48
	v_ashrrev_i32_e32 v35, 31, v34
	v_lshlrev_b64 v[34:35], 11, v[34:35]
	v_cvt_pk_bf16_f32 v33, v71, v73
	ds_read2_b32 v[38:39], v47 offset0:16 offset1:24
	v_lshl_add_u64 v[34:35], v[36:37], 0, v[34:35]
	global_store_dwordx4 v[34:35], v[30:33], off
	ds_read2_b32 v[34:35], v47 offset0:49 offset1:57
	ds_read2_b32 v[40:41], v47 offset0:82 offset1:90
	ds_read2_b32 v[42:43], v47 offset0:115 offset1:123
	s_waitcnt lgkmcnt(3)
	s_waitcnt lgkmcnt(2)
	ds_read2_b32 v[44:45], v47 offset0:148 offset1:156
	ds_read2_b32 v[68:69], v47 offset0:181 offset1:189
	v_cvt_pk_bf16_f32 v30, v38, v34
	s_waitcnt lgkmcnt(3)
	s_waitcnt lgkmcnt(2)
	ds_read2_b32 v[70:71], v47 offset0:214 offset1:222
	ds_read2_b32 v[72:73], v47 offset0:247 offset1:255
	v_cvt_pk_bf16_f32 v31, v40, v42
	s_waitcnt lgkmcnt(3)
	s_waitcnt lgkmcnt(2)
	v_cvt_pk_bf16_f32 v32, v44, v68
	s_waitcnt lgkmcnt(1)
	v_add_u32_e32 v74, s6, v49
	s_waitcnt lgkmcnt(0)
	v_ashrrev_i32_e32 v75, 31, v74
	v_lshlrev_b64 v[74:75], 11, v[74:75]
	v_cvt_pk_bf16_f32 v33, v70, v72
	v_lshl_add_u64 v[74:75], v[36:37], 0, v[74:75]
	global_store_dwordx4 v[74:75], v[30:33], off
	s_nop 1
	v_cvt_pk_bf16_f32 v30, v39, v35
	v_cvt_pk_bf16_f32 v31, v41, v43
	v_cvt_pk_bf16_f32 v32, v45, v69
	v_add_u32_e32 v34, s6, v50
	v_ashrrev_i32_e32 v35, 31, v34
	v_lshlrev_b64 v[34:35], 11, v[34:35]
	v_cvt_pk_bf16_f32 v33, v71, v73
	v_lshl_add_u64 v[34:35], v[36:37], 0, v[34:35]
	global_store_dwordx4 v[34:35], v[30:33], off
	s_waitcnt lgkmcnt(0)

.LBB0_60:
	v_lshl_add_u64 v[68:69], v[44:45], 0, s[6:7]
	v_lshl_add_u64 v[70:71], v[42:43], 0, s[6:7]
	v_lshl_add_u64 v[72:73], v[40:41], 0, s[6:7]
	v_lshl_add_u64 v[74:75], v[38:39], 0, s[6:7]
	v_lshl_add_u64 v[76:77], v[36:37], 0, s[6:7]
	v_lshl_add_u64 v[78:79], v[34:35], 0, s[6:7]
	v_lshl_add_u64 v[80:81], v[32:33], 0, s[6:7]
	v_lshl_add_u64 v[82:83], v[30:31], 0, s[6:7]
	global_load_dword v120, v[68:69], off nt
	global_load_dword v121, v[70:71], off nt
	global_load_dword v122, v[72:73], off nt
	global_load_dword v123, v[74:75], off nt
	global_load_dword v124, v[76:77], off nt
	global_load_dword v125, v[78:79], off nt
	global_load_dword v126, v[80:81], off nt
	global_load_dword v127, v[82:83], off nt
	s_add_u32 s6, s6, 0x10000
	s_addc_u32 s7, s7, 0
	v_lshl_add_u64 v[152:153], v[44:45], 0, s[6:7]
	v_lshl_add_u64 v[154:155], v[42:43], 0, s[6:7]
	v_lshl_add_u64 v[156:157], v[40:41], 0, s[6:7]
	v_lshl_add_u64 v[158:159], v[38:39], 0, s[6:7]
	v_lshl_add_u64 v[160:161], v[36:37], 0, s[6:7]
	v_lshl_add_u64 v[162:163], v[34:35], 0, s[6:7]
	v_lshl_add_u64 v[164:165], v[32:33], 0, s[6:7]
	v_lshl_add_u64 v[166:167], v[30:31], 0, s[6:7]
	global_load_dword v128, v[152:153], off nt
	global_load_dword v129, v[154:155], off nt
	global_load_dword v130, v[156:157], off nt
	global_load_dword v131, v[158:159], off nt
	global_load_dword v132, v[160:161], off nt
	global_load_dword v133, v[162:163], off nt
	global_load_dword v134, v[164:165], off nt
	global_load_dword v135, v[166:167], off nt
	s_add_u32 s6, s6, 0x10000
	s_addc_u32 s7, s7, 0
	v_lshl_add_u64 v[168:169], v[44:45], 0, s[6:7]
	v_lshl_add_u64 v[170:171], v[42:43], 0, s[6:7]
	v_lshl_add_u64 v[172:173], v[40:41], 0, s[6:7]
	v_lshl_add_u64 v[174:175], v[38:39], 0, s[6:7]
	v_lshl_add_u64 v[176:177], v[36:37], 0, s[6:7]
	v_lshl_add_u64 v[178:179], v[34:35], 0, s[6:7]
	v_lshl_add_u64 v[180:181], v[32:33], 0, s[6:7]
	v_lshl_add_u64 v[182:183], v[30:31], 0, s[6:7]
	global_load_dword v136, v[168:169], off nt
	global_load_dword v137, v[170:171], off nt
	global_load_dword v138, v[172:173], off nt
	global_load_dword v139, v[174:175], off nt
	global_load_dword v140, v[176:177], off nt
	global_load_dword v141, v[178:179], off nt
	global_load_dword v142, v[180:181], off nt
	global_load_dword v143, v[182:183], off nt
	s_add_u32 s6, s6, 0x10000
	s_addc_u32 s7, s7, 0
	v_lshl_add_u64 v[184:185], v[44:45], 0, s[6:7]
	v_lshl_add_u64 v[186:187], v[42:43], 0, s[6:7]
	v_lshl_add_u64 v[188:189], v[40:41], 0, s[6:7]
	v_lshl_add_u64 v[190:191], v[38:39], 0, s[6:7]
	v_lshl_add_u64 v[192:193], v[36:37], 0, s[6:7]
	v_lshl_add_u64 v[194:195], v[34:35], 0, s[6:7]
	v_lshl_add_u64 v[196:197], v[32:33], 0, s[6:7]
	v_lshl_add_u64 v[198:199], v[30:31], 0, s[6:7]
	global_load_dword v144, v[184:185], off nt
	global_load_dword v145, v[186:187], off nt
	global_load_dword v146, v[188:189], off nt
	global_load_dword v147, v[190:191], off nt
	global_load_dword v148, v[192:193], off nt
	global_load_dword v149, v[194:195], off nt
	global_load_dword v150, v[196:197], off nt
	global_load_dword v151, v[198:199], off nt
	s_add_u32 s6, s6, 0x10000
	s_addc_u32 s7, s7, 0
	v_add_u32_e32 v75, 0x400, v8
	s_waitcnt vmcnt(30)
	ds_write2_b32 v8, v120, v121 offset1:66
	s_waitcnt vmcnt(28)
	ds_write2_b32 v8, v122, v123 offset0:132 offset1:198
	s_waitcnt vmcnt(26)
	ds_write2_b32 v75, v124, v125 offset0:8 offset1:74
	s_waitcnt vmcnt(24)
	ds_write2_b32 v75, v126, v127 offset0:140 offset1:206
	v_add_u32_e32 v8, 0x840, v8
	v_add_u32_e32 v75, 0x400, v8
	s_waitcnt vmcnt(22)
	ds_write2_b32 v8, v128, v129 offset1:66
	s_waitcnt vmcnt(20)
	ds_write2_b32 v8, v130, v131 offset0:132 offset1:198
	s_waitcnt vmcnt(18)
	ds_write2_b32 v75, v132, v133 offset0:8 offset1:74
	s_waitcnt vmcnt(16)
	ds_write2_b32 v75, v134, v135 offset0:140 offset1:206
	v_add_u32_e32 v8, 0x840, v8
	v_add_u32_e32 v75, 0x400, v8
	s_waitcnt vmcnt(14)
	ds_write2_b32 v8, v136, v137 offset1:66
	s_waitcnt vmcnt(12)
	ds_write2_b32 v8, v138, v139 offset0:132 offset1:198
	s_waitcnt vmcnt(10)
	ds_write2_b32 v75, v140, v141 offset0:8 offset1:74
	s_waitcnt vmcnt(8)
	ds_write2_b32 v75, v142, v143 offset0:140 offset1:206
	v_add_u32_e32 v8, 0x840, v8
	v_add_u32_e32 v75, 0x400, v8
	s_waitcnt vmcnt(6)
	ds_write2_b32 v8, v144, v145 offset1:66
	s_waitcnt vmcnt(4)
	ds_write2_b32 v8, v146, v147 offset0:132 offset1:198
	s_waitcnt vmcnt(2)
	ds_write2_b32 v75, v148, v149 offset0:8 offset1:74
	s_waitcnt vmcnt(0)
	ds_write2_b32 v75, v150, v151 offset0:140 offset1:206
	v_add_u32_e32 v8, 0x840, v8
	s_cmp_lg_u32 s6, 0x40000
	s_lshr_b32 s0, s0, 9
	s_lshl_b32 s6, s46, 5
	s_waitcnt lgkmcnt(0)
	s_and_b32 s8, s6, 0x3e0
	s_lshl_b64 s[6:7], s[0:1], 21
	ds_read2_b32 v[34:35], v47 offset1:8
	s_add_u32 s0, s24, s6
	ds_read2_b32 v[38:39], v47 offset0:33 offset1:41
	s_addc_u32 s7, s25, s7
	s_lshl_b32 s6, s9, 1
	s_add_u32 s6, s0, s6
	ds_read2_b32 v[40:41], v47 offset0:66 offset1:74
	s_addc_u32 s7, s7, 0
	v_lshlrev_b32_e32 v8, 1, v12
	ds_read2_b32 v[42:43], v47 offset0:99 offset1:107
	v_lshl_add_u64 v[36:37], s[6:7], 0, v[8:9]
	s_waitcnt lgkmcnt(3)
	s_waitcnt lgkmcnt(2)
	ds_read2_b32 v[44:45], v47 offset0:132 offset1:140
	ds_read2_b32 v[68:69], v47 offset0:165 offset1:173
	v_cvt_pk_bf16_f32 v30, v34, v38
	s_waitcnt lgkmcnt(3)
	s_waitcnt lgkmcnt(2)
	ds_read2_b32 v[70:71], v47 offset0:198 offset1:206
	ds_read2_b32 v[72:73], v47 offset0:231 offset1:239
	v_cvt_pk_bf16_f32 v31, v40, v42
	s_waitcnt lgkmcnt(3)
	s_waitcnt lgkmcnt(2)
	v_cvt_pk_bf16_f32 v32, v44, v68
	s_waitcnt lgkmcnt(1)
	v_add_u32_e32 v74, s8, v46
	s_waitcnt lgkmcnt(0)
	v_ashrrev_i32_e32 v75, 31, v74
	v_lshlrev_b64 v[74:75], 11, v[74:75]
	v_cvt_pk_bf16_f32 v33, v70, v72
	v_lshl_add_u64 v[74:75], v[36:37], 0, v[74:75]
	global_store_dwordx4 v[74:75], v[30:33], off
	s_nop 1
	v_cvt_pk_bf16_f32 v30, v35, v39
	v_cvt_pk_bf16_f32 v31, v41, v43
	v_cvt_pk_bf16_f32 v32, v45, v69
	v_add_u32_e32 v34, s8, v48
	v_ashrrev_i32_e32 v35, 31, v34
	v_lshlrev_b64 v[34:35], 11, v[34:35]
	v_cvt_pk_bf16_f32 v33, v71, v73
	ds_read2_b32 v[38:39], v47 offset0:16 offset1:24
	v_lshl_add_u64 v[34:35], v[36:37], 0, v[34:35]
	global_store_dwordx4 v[34:35], v[30:33], off
	ds_read2_b32 v[34:35], v47 offset0:49 offset1:57
	ds_read2_b32 v[40:41], v47 offset0:82 offset1:90
	ds_read2_b32 v[42:43], v47 offset0:115 offset1:123
	s_waitcnt lgkmcnt(3)
	s_waitcnt lgkmcnt(2)
	ds_read2_b32 v[44:45], v47 offset0:148 offset1:156
	ds_read2_b32 v[68:69], v47 offset0:181 offset1:189
	v_cvt_pk_bf16_f32 v30, v38, v34
	s_waitcnt lgkmcnt(3)
	s_waitcnt lgkmcnt(2)
	ds_read2_b32 v[70:71], v47 offset0:214 offset1:222
	ds_read2_b32 v[72:73], v47 offset0:247 offset1:255
	v_cvt_pk_bf16_f32 v31, v40, v42
	s_waitcnt lgkmcnt(3)
	s_waitcnt lgkmcnt(2)
	v_cvt_pk_bf16_f32 v32, v44, v68
	s_waitcnt lgkmcnt(1)
	v_add_u32_e32 v74, s8, v49
	s_waitcnt lgkmcnt(0)
	v_ashrrev_i32_e32 v75, 31, v74
	v_lshlrev_b64 v[74:75], 11, v[74:75]
	v_cvt_pk_bf16_f32 v33, v70, v72
	v_lshl_add_u64 v[74:75], v[36:37], 0, v[74:75]
	global_store_dwordx4 v[74:75], v[30:33], off
	s_nop 1
	v_cvt_pk_bf16_f32 v30, v39, v35
	v_cvt_pk_bf16_f32 v31, v41, v43
	v_cvt_pk_bf16_f32 v32, v45, v69
	v_add_u32_e32 v34, s8, v50
	v_ashrrev_i32_e32 v35, 31, v34
	v_lshlrev_b64 v[34:35], 11, v[34:35]
	v_cvt_pk_bf16_f32 v33, v71, v73
	v_lshl_add_u64 v[34:35], v[36:37], 0, v[34:35]
	global_store_dwordx4 v[34:35], v[30:33], off
	s_waitcnt lgkmcnt(0)

.LBB0_65:
	v_lshl_add_u64 v[68:69], v[44:45], 0, s[10:11]
	v_lshl_add_u64 v[70:71], v[42:43], 0, s[10:11]
	v_lshl_add_u64 v[72:73], v[40:41], 0, s[10:11]
	v_lshl_add_u64 v[74:75], v[38:39], 0, s[10:11]
	v_lshl_add_u64 v[76:77], v[36:37], 0, s[10:11]
	v_lshl_add_u64 v[78:79], v[34:35], 0, s[10:11]
	v_lshl_add_u64 v[80:81], v[32:33], 0, s[10:11]
	v_lshl_add_u64 v[82:83], v[30:31], 0, s[10:11]
	global_load_dword v120, v[68:69], off nt
	global_load_dword v121, v[70:71], off nt
	global_load_dword v122, v[72:73], off nt
	global_load_dword v123, v[74:75], off nt
	global_load_dword v124, v[76:77], off nt
	global_load_dword v125, v[78:79], off nt
	global_load_dword v126, v[80:81], off nt
	global_load_dword v127, v[82:83], off nt
	s_add_u32 s10, s10, 0x24000
	s_addc_u32 s11, s11, 0
	v_lshl_add_u64 v[152:153], v[44:45], 0, s[10:11]
	v_lshl_add_u64 v[154:155], v[42:43], 0, s[10:11]
	v_lshl_add_u64 v[156:157], v[40:41], 0, s[10:11]
	v_lshl_add_u64 v[158:159], v[38:39], 0, s[10:11]
	v_lshl_add_u64 v[160:161], v[36:37], 0, s[10:11]
	v_lshl_add_u64 v[162:163], v[34:35], 0, s[10:11]
	v_lshl_add_u64 v[164:165], v[32:33], 0, s[10:11]
	v_lshl_add_u64 v[166:167], v[30:31], 0, s[10:11]
	global_load_dword v128, v[152:153], off nt
	global_load_dword v129, v[154:155], off nt
	global_load_dword v130, v[156:157], off nt
	global_load_dword v131, v[158:159], off nt
	global_load_dword v132, v[160:161], off nt
	global_load_dword v133, v[162:163], off nt
	global_load_dword v134, v[164:165], off nt
	global_load_dword v135, v[166:167], off nt
	s_add_u32 s10, s10, 0x24000
	s_addc_u32 s11, s11, 0
	v_lshl_add_u64 v[168:169], v[44:45], 0, s[10:11]
	v_lshl_add_u64 v[170:171], v[42:43], 0, s[10:11]
	v_lshl_add_u64 v[172:173], v[40:41], 0, s[10:11]
	v_lshl_add_u64 v[174:175], v[38:39], 0, s[10:11]
	v_lshl_add_u64 v[176:177], v[36:37], 0, s[10:11]
	v_lshl_add_u64 v[178:179], v[34:35], 0, s[10:11]
	v_lshl_add_u64 v[180:181], v[32:33], 0, s[10:11]
	v_lshl_add_u64 v[182:183], v[30:31], 0, s[10:11]
	global_load_dword v136, v[168:169], off nt
	global_load_dword v137, v[170:171], off nt
	global_load_dword v138, v[172:173], off nt
	global_load_dword v139, v[174:175], off nt
	global_load_dword v140, v[176:177], off nt
	global_load_dword v141, v[178:179], off nt
	global_load_dword v142, v[180:181], off nt
	global_load_dword v143, v[182:183], off nt
	s_add_u32 s10, s10, 0x24000
	s_addc_u32 s11, s11, 0
	v_lshl_add_u64 v[184:185], v[44:45], 0, s[10:11]
	v_lshl_add_u64 v[186:187], v[42:43], 0, s[10:11]
	v_lshl_add_u64 v[188:189], v[40:41], 0, s[10:11]
	v_lshl_add_u64 v[190:191], v[38:39], 0, s[10:11]
	v_lshl_add_u64 v[192:193], v[36:37], 0, s[10:11]
	v_lshl_add_u64 v[194:195], v[34:35], 0, s[10:11]
	v_lshl_add_u64 v[196:197], v[32:33], 0, s[10:11]
	v_lshl_add_u64 v[198:199], v[30:31], 0, s[10:11]
	global_load_dword v144, v[184:185], off nt
	global_load_dword v145, v[186:187], off nt
	global_load_dword v146, v[188:189], off nt
	global_load_dword v147, v[190:191], off nt
	global_load_dword v148, v[192:193], off nt
	global_load_dword v149, v[194:195], off nt
	global_load_dword v150, v[196:197], off nt
	global_load_dword v151, v[198:199], off nt
	s_add_u32 s10, s10, 0x24000
	s_addc_u32 s11, s11, 0
	v_add_u32_e32 v75, 0x400, v8
	s_waitcnt vmcnt(30)
	ds_write2_b32 v8, v120, v121 offset1:66
	s_waitcnt vmcnt(28)
	ds_write2_b32 v8, v122, v123 offset0:132 offset1:198
	s_waitcnt vmcnt(26)
	ds_write2_b32 v75, v124, v125 offset0:8 offset1:74
	s_waitcnt vmcnt(24)
	ds_write2_b32 v75, v126, v127 offset0:140 offset1:206
	v_add_u32_e32 v8, 0x840, v8
	v_add_u32_e32 v75, 0x400, v8
	s_waitcnt vmcnt(22)
	ds_write2_b32 v8, v128, v129 offset1:66
	s_waitcnt vmcnt(20)
	ds_write2_b32 v8, v130, v131 offset0:132 offset1:198
	s_waitcnt vmcnt(18)
	ds_write2_b32 v75, v132, v133 offset0:8 offset1:74
	s_waitcnt vmcnt(16)
	ds_write2_b32 v75, v134, v135 offset0:140 offset1:206
	v_add_u32_e32 v8, 0x840, v8
	v_add_u32_e32 v75, 0x400, v8
	s_waitcnt vmcnt(14)
	ds_write2_b32 v8, v136, v137 offset1:66
	s_waitcnt vmcnt(12)
	ds_write2_b32 v8, v138, v139 offset0:132 offset1:198
	s_waitcnt vmcnt(10)
	ds_write2_b32 v75, v140, v141 offset0:8 offset1:74
	s_waitcnt vmcnt(8)
	ds_write2_b32 v75, v142, v143 offset0:140 offset1:206
	v_add_u32_e32 v8, 0x840, v8
	v_add_u32_e32 v75, 0x400, v8
	s_waitcnt vmcnt(6)
	ds_write2_b32 v8, v144, v145 offset1:66
	s_waitcnt vmcnt(4)
	ds_write2_b32 v8, v146, v147 offset0:132 offset1:198
	s_waitcnt vmcnt(2)
	ds_write2_b32 v75, v148, v149 offset0:8 offset1:74
	s_waitcnt vmcnt(0)
	ds_write2_b32 v75, v150, v151 offset0:140 offset1:206
	v_add_u32_e32 v8, 0x840, v8
	s_cmp_lg_u32 s10, 0x90000
	s_waitcnt lgkmcnt(0)
	s_mul_hi_i32 s7, s0, 0x480000
	s_mul_i32 s0, s0, 0x480000
	ds_read2_b32 v[34:35], v47 offset1:8
	s_add_u32 s0, s26, s0
	ds_read2_b32 v[38:39], v47 offset0:33 offset1:41
	s_addc_u32 s7, s27, s7
	s_lshl_b64 s[8:9], s[8:9], 1
	s_add_u32 s8, s0, s8
	ds_read2_b32 v[40:41], v47 offset0:66 offset1:74
	s_addc_u32 s9, s7, s9
	v_lshlrev_b32_e32 v8, 1, v12
	ds_read2_b32 v[42:43], v47 offset0:99 offset1:107
	v_lshl_add_u64 v[36:37], s[8:9], 0, v[8:9]
	s_waitcnt lgkmcnt(3)
	s_waitcnt lgkmcnt(2)
	ds_read2_b32 v[44:45], v47 offset0:132 offset1:140
	ds_read2_b32 v[68:69], v47 offset0:165 offset1:173
	v_cvt_pk_bf16_f32 v30, v34, v38
	s_waitcnt lgkmcnt(3)
	s_waitcnt lgkmcnt(2)
	ds_read2_b32 v[70:71], v47 offset0:198 offset1:206
	ds_read2_b32 v[72:73], v47 offset0:231 offset1:239
	v_cvt_pk_bf16_f32 v31, v40, v42
	s_waitcnt lgkmcnt(3)
	s_waitcnt lgkmcnt(2)
	v_cvt_pk_bf16_f32 v32, v44, v68
	s_waitcnt lgkmcnt(1)
	v_add_u32_e32 v74, s6, v46
	s_waitcnt lgkmcnt(0)
	v_ashrrev_i32_e32 v75, 31, v74
	v_lshlrev_b64 v[74:75], 11, v[74:75]
	v_cvt_pk_bf16_f32 v33, v70, v72
	v_lshl_add_u64 v[74:75], v[36:37], 0, v[74:75]
	global_store_dwordx4 v[74:75], v[30:33], off
	s_nop 1
	v_cvt_pk_bf16_f32 v30, v35, v39
	v_cvt_pk_bf16_f32 v31, v41, v43
	v_cvt_pk_bf16_f32 v32, v45, v69
	v_add_u32_e32 v34, s6, v48
	v_ashrrev_i32_e32 v35, 31, v34
	v_lshlrev_b64 v[34:35], 11, v[34:35]
	v_cvt_pk_bf16_f32 v33, v71, v73
	ds_read2_b32 v[38:39], v47 offset0:16 offset1:24
	v_lshl_add_u64 v[34:35], v[36:37], 0, v[34:35]
	global_store_dwordx4 v[34:35], v[30:33], off
	ds_read2_b32 v[34:35], v47 offset0:49 offset1:57
	ds_read2_b32 v[40:41], v47 offset0:82 offset1:90
	ds_read2_b32 v[42:43], v47 offset0:115 offset1:123
	s_waitcnt lgkmcnt(3)
	s_waitcnt lgkmcnt(2)
	ds_read2_b32 v[44:45], v47 offset0:148 offset1:156
	ds_read2_b32 v[68:69], v47 offset0:181 offset1:189
	v_cvt_pk_bf16_f32 v30, v38, v34
	s_waitcnt lgkmcnt(3)
	s_waitcnt lgkmcnt(2)
	ds_read2_b32 v[70:71], v47 offset0:214 offset1:222
	ds_read2_b32 v[72:73], v47 offset0:247 offset1:255
	v_cvt_pk_bf16_f32 v31, v40, v42
	s_waitcnt lgkmcnt(3)
	s_waitcnt lgkmcnt(2)
	v_cvt_pk_bf16_f32 v32, v44, v68
	s_waitcnt lgkmcnt(1)
	v_add_u32_e32 v74, s6, v49
	s_waitcnt lgkmcnt(0)
	v_ashrrev_i32_e32 v75, 31, v74
	v_lshlrev_b64 v[74:75], 11, v[74:75]
	v_cvt_pk_bf16_f32 v33, v70, v72
	v_lshl_add_u64 v[74:75], v[36:37], 0, v[74:75]
	global_store_dwordx4 v[74:75], v[30:33], off
	s_nop 1
	v_cvt_pk_bf16_f32 v30, v39, v35
	v_cvt_pk_bf16_f32 v31, v41, v43
	v_cvt_pk_bf16_f32 v32, v45, v69
	v_add_u32_e32 v34, s6, v50
	v_ashrrev_i32_e32 v35, 31, v34
	v_lshlrev_b64 v[34:35], 11, v[34:35]
	v_cvt_pk_bf16_f32 v33, v71, v73
	v_lshl_add_u64 v[34:35], v[36:37], 0, v[34:35]
	global_store_dwordx4 v[34:35], v[30:33], off
	s_waitcnt lgkmcnt(0)
	s_branch .LBB0_34
